# v25: v23 + spatial gating: LN(v) rows permuted in LDS so each lane owns 8 contiguous channels per block pair: u read by 4x16-byte loads and result written by 4x16-byte stores per lane (was 8x8-byte ea
# speedup vs baseline: 1.0143x; 1.0143x over previous
; __device__ __forceinline__ unsigned cvt_pk_bf16(float lo, float hi) { unsigned r; asm volatile("v_cvt_pk_bf16_f32 %0, %1, %2" : "=v"(r) : "v"(lo), "v"(hi)); return r; }
; __device__ __forceinline__ void sg_phase(const Frame& F, const KArgs& a, const int u_first, const int u_count) {
;     ...
; #pragma unroll
;         for (int j = 0; j < 8; ++j) { const int ch = 16 * j + 4 * kq; const u32x2 uu = uraw[j];
;             const float o0 = __builtin_bit_cast(float, uu.x << 16) * (acc[j][0] + bs), o1 = __builtin_bit_cast(float, uu.x & 0xffff0000u) * (acc[j][1] + bs);
;             const float o2 = __builtin_bit_cast(float, uu.y << 16) * (acc[j][2] + bs), o3 = __builtin_bit_cast(float, uu.y & 0xffff0000u) * (acc[j][3] + bs);
;             u32x2 o; o.x = cvt_pk_bf16(o0, o1); o.y = cvt_pk_bf16(o2, o3); *(u32x2*)(AS + (size_t)(t0 + t) * DM + FW + g * 128 + ch) = o; }
;         __syncthreads();
;     }
.LBB0_803:
	s_waitcnt vmcnt(0)
	v_lshlrev_b64 v[34:35], 12, v[174:175]
	v_lshl_add_u64 v[34:35], s[72:73], 0, v[34:35]
	v_lshl_add_u64 v[34:35], v[34:35], 0, s[78:79]
	v_mov_b32_e32 v157, v147
	v_lshl_add_u64 v[34:35], v[34:35], 0, v[156:157]
	s_mov_b64 s[70:71], 0x17800800
	v_lshl_add_u64 v[38:39], v[34:35], 0, s[70:71]
	v_lshl_add_u64 v[38:39], v[38:39], 0, v[156:157]
	v_lshlrev_b32_e32 v34, 16, v170
	v_add_f32_e32 v35, v146, v82
	v_mul_f32_e32 v34, v35, v34
	v_and_b32_e32 v35, 0xffff0000, v170
	v_add_f32_e32 v36, v146, v83
	v_mul_f32_e32 v35, v36, v35
	v_lshlrev_b32_e32 v36, 16, v171
	v_add_f32_e32 v37, v146, v84
	v_mul_f32_e32 v36, v37, v36
	v_and_b32_e32 v37, 0xffff0000, v171
	v_add_f32_e32 v40, v146, v85
	v_mul_f32_e32 v37, v40, v37
	v_cvt_pk_bf16_f32 v170, v34, v35
	v_cvt_pk_bf16_f32 v171, v36, v37
	v_lshlrev_b32_e32 v34, 16, v172
	v_add_f32_e32 v35, v146, v86
	v_mul_f32_e32 v34, v35, v34
	v_and_b32_e32 v35, 0xffff0000, v172
	v_add_f32_e32 v36, v146, v87
	v_mul_f32_e32 v35, v36, v35
	v_lshlrev_b32_e32 v36, 16, v173
	v_add_f32_e32 v37, v146, v88
	v_mul_f32_e32 v36, v37, v36
	v_and_b32_e32 v37, 0xffff0000, v173
	v_add_f32_e32 v40, v146, v89
	v_mul_f32_e32 v37, v40, v37
	v_cvt_pk_bf16_f32 v172, v34, v35
	v_cvt_pk_bf16_f32 v173, v36, v37
	s_nop 0
	global_store_dwordx4 v[38:39], v[170:173], off
	v_lshlrev_b32_e32 v34, 16, v166
	v_add_f32_e32 v35, v146, v74
	v_mul_f32_e32 v34, v35, v34
	v_and_b32_e32 v35, 0xffff0000, v166
	v_add_f32_e32 v36, v146, v75
	v_mul_f32_e32 v35, v36, v35
	v_lshlrev_b32_e32 v36, 16, v167
	v_add_f32_e32 v37, v146, v76
	v_mul_f32_e32 v36, v37, v36
	v_and_b32_e32 v37, 0xffff0000, v167
	v_add_f32_e32 v40, v146, v77
	v_mul_f32_e32 v37, v40, v37
	v_cvt_pk_bf16_f32 v166, v34, v35
	v_cvt_pk_bf16_f32 v167, v36, v37
	v_lshlrev_b32_e32 v34, 16, v168
	v_add_f32_e32 v35, v146, v78
	v_mul_f32_e32 v34, v35, v34
	v_and_b32_e32 v35, 0xffff0000, v168
	v_add_f32_e32 v36, v146, v79
	v_mul_f32_e32 v35, v36, v35
	v_lshlrev_b32_e32 v36, 16, v169
	v_add_f32_e32 v37, v146, v80
	v_mul_f32_e32 v36, v37, v36
	v_and_b32_e32 v37, 0xffff0000, v169
	v_add_f32_e32 v40, v146, v81
	v_mul_f32_e32 v37, v40, v37
	v_cvt_pk_bf16_f32 v168, v34, v35
	v_cvt_pk_bf16_f32 v169, v36, v37
	s_nop 0
	global_store_dwordx4 v[38:39], v[166:169], off offset:64
	v_lshlrev_b32_e32 v34, 16, v162
	v_add_f32_e32 v35, v146, v66
	v_mul_f32_e32 v34, v35, v34
	v_and_b32_e32 v35, 0xffff0000, v162
	v_add_f32_e32 v36, v146, v67
	v_mul_f32_e32 v35, v36, v35
	v_lshlrev_b32_e32 v36, 16, v163
	v_add_f32_e32 v37, v146, v68
	v_mul_f32_e32 v36, v37, v36
	v_and_b32_e32 v37, 0xffff0000, v163
	v_add_f32_e32 v40, v146, v69
	v_mul_f32_e32 v37, v40, v37
	v_cvt_pk_bf16_f32 v162, v34, v35
	v_cvt_pk_bf16_f32 v163, v36, v37
	v_lshlrev_b32_e32 v34, 16, v164
	v_add_f32_e32 v35, v146, v70
	v_mul_f32_e32 v34, v35, v34
	v_and_b32_e32 v35, 0xffff0000, v164
	v_add_f32_e32 v36, v146, v71
	v_mul_f32_e32 v35, v36, v35
	v_lshlrev_b32_e32 v36, 16, v165
	v_add_f32_e32 v37, v146, v72
	v_mul_f32_e32 v36, v37, v36
	v_and_b32_e32 v37, 0xffff0000, v165
	v_add_f32_e32 v40, v146, v73
	v_mul_f32_e32 v37, v40, v37
	v_cvt_pk_bf16_f32 v164, v34, v35
	v_cvt_pk_bf16_f32 v165, v36, v37
	s_nop 0
	global_store_dwordx4 v[38:39], v[162:165], off offset:128
	v_lshlrev_b32_e32 v34, 16, v158
	v_add_f32_e32 v35, v146, v58
	v_mul_f32_e32 v34, v35, v34
	v_and_b32_e32 v35, 0xffff0000, v158
	v_add_f32_e32 v36, v146, v59
	v_mul_f32_e32 v35, v36, v35
	v_lshlrev_b32_e32 v36, 16, v159
	v_add_f32_e32 v37, v146, v60
	v_mul_f32_e32 v36, v37, v36
	v_and_b32_e32 v37, 0xffff0000, v159
	v_add_f32_e32 v40, v146, v61
	v_mul_f32_e32 v37, v40, v37
	v_cvt_pk_bf16_f32 v158, v34, v35
	v_cvt_pk_bf16_f32 v159, v36, v37
	v_lshlrev_b32_e32 v34, 16, v160
	v_add_f32_e32 v35, v146, v62
	v_mul_f32_e32 v34, v35, v34
	v_and_b32_e32 v35, 0xffff0000, v160
	v_add_f32_e32 v36, v146, v63
	v_mul_f32_e32 v35, v36, v35
	v_lshlrev_b32_e32 v36, 16, v161
	v_add_f32_e32 v37, v146, v64
	v_mul_f32_e32 v36, v37, v36
	v_and_b32_e32 v37, 0xffff0000, v161
	v_add_f32_e32 v40, v146, v65
	v_mul_f32_e32 v37, v40, v37
	v_cvt_pk_bf16_f32 v160, v34, v35
	v_cvt_pk_bf16_f32 v161, v36, v37
	s_nop 0
	global_store_dwordx4 v[38:39], v[158:161], off offset:192
	v_add_u32_e32 v1, -1, v1
	v_cmp_ne_u32_e32 vcc, 0, v1
	s_addk_i32 s33, 0x80
	s_and_b64 vcc, exec, vcc
	s_add_i32 s90, s90, 16
	s_barrier
	s_cbranch_vccz .LBB0_820

; __device__ __forceinline__ unsigned f2bf(float f) { unsigned u = __builtin_bit_cast(unsigned, f); return (u + 0x7fffu + ((u >> 16) & 1u)) >> 16; }
; __device__ __forceinline__ void sg_phase(const Frame& F, const KArgs& a, const int u_first, const int u_count) {
;     ...
;         u32x2 uraw[8];
; #pragma unroll
;         for (int j = 0; j < 8; ++j) uraw[j] = *(const u32x2*)(ZU + (size_t)(t0 + t) * SGW + g * 128 + 16 * j + 4 * kq);
;         const float bs = b_sp[g * 128 + t];
;         if (tid < 128) { float S = 0.f, Q = 0.f;
; #pragma unroll
;             for (int i = 0; i < 8; ++i) { const f32x4 v = zst[i]; S += v[0] + v[2]; Q += v[1] + v[3]; }
;             const float mu = S * (1.f / SGW), var = fmaxf(Q * (1.f / SGW) - mu * mu, 0.f); st[tid] = (f32x2){mu, rsqrtf(var + LN_EPS)}; }
;         __syncthreads();
;         { const int s = s_; const f32x2 ms = st[s];
; #pragma unroll
;             for (int q = 0; q < 4; ++q) { const u32x4 raw = zraw[q]; const unsigned rw[4] = {raw.x, raw.y, raw.z, raw.w};
;                 const f32x4 g0 = lg[q][0], g1 = lg[q][1], b0 = lb[q][0], b1 = lb[q][1];
; #pragma unroll
;                 for (int i = 0; i < 8; ++i) { const unsigned wd = rw[i >> 1]; const float v = __builtin_bit_cast(float, (i & 1) ? (wd & 0xffff0000u) : (wd << 16));
;                     const float gg = (i < 4) ? g0[i & 3] : g1[i & 3], bb = (i < 4) ? b0[i & 3] : b1[i & 3];
;                     vt[(c0 + 8 * q + i) * 136 + (s ^ ((tid & 3) * 16))] = (unsigned short)f2bf((v - ms[0]) * ms[1] * gg + bb); } } }
.LBB0_812:
	v_add_u32_e32 v174, s76, v176
	v_ashrrev_i32_e32 v175, 31, v174
	v_lshlrev_b64 v[158:159], 11, v[174:175]
	v_lshl_add_u64 v[158:159], s[0:1], 0, v[158:159]
	v_lshl_add_u64 v[158:159], v[158:159], 0, s[78:79]
	v_mov_b32_e32 v157, v147
	v_lshl_add_u64 v[158:159], v[158:159], 0, v[156:157]
	v_lshl_add_u64 v[158:159], v[158:159], 0, v[156:157]
	global_load_dwordx4 v[170:173], v[158:159], off
	global_load_dwordx4 v[166:169], v[158:159], off offset:64
	global_load_dwordx4 v[162:165], v[158:159], off offset:128
	s_nop 0
	global_load_dwordx4 v[158:161], v[158:159], off offset:192
	v_readlane_b32 s36, v252, 47
	v_readlane_b32 s37, v252, 48
	v_readlane_b32 s38, v252, 49
	v_readlane_b32 s39, v252, 50
	v_lshl_add_u64 v[184:185], v[146:147], 2, s[36:37]
	global_load_dword v146, v[184:185], off
	v_readlane_b32 s40, v252, 51
	v_readlane_b32 s41, v252, 52
	v_readlane_b32 s42, v252, 53
	v_readlane_b32 s43, v252, 54
	v_readlane_b32 s44, v252, 55
	v_readlane_b32 s45, v252, 56
	v_readlane_b32 s46, v252, 57
	v_readlane_b32 s47, v252, 58
	v_readlane_b32 s48, v252, 59
	v_readlane_b32 s49, v252, 60
	v_readlane_b32 s50, v252, 61
	v_readlane_b32 s51, v252, 62
	s_and_saveexec_b64 s[76:77], s[2:3]
	s_cbranch_execz .LBB0_814
	s_waitcnt vmcnt(17)
	v_pk_add_f32 v[184:185], v[2:3], v[4:5]
	v_pk_add_f32 v[186:187], v[6:7], v[8:9]
	v_pk_add_f32 v[184:185], v[184:185], 0 op_sel_hi:[1,0]
	s_mov_b32 s92, 0x3a800000
	v_pk_add_f32 v[184:185], v[184:185], v[186:187]
	v_pk_add_f32 v[186:187], v[10:11], v[12:13]
	s_nop 0
	v_pk_add_f32 v[184:185], v[184:185], v[186:187]
	v_pk_add_f32 v[186:187], v[14:15], v[16:17]
	s_nop 0
	v_pk_add_f32 v[184:185], v[184:185], v[186:187]
	s_waitcnt vmcnt(13)
	v_pk_add_f32 v[186:187], v[18:19], v[20:21]
	s_nop 0
	v_pk_add_f32 v[184:185], v[184:185], v[186:187]
	v_pk_add_f32 v[186:187], v[22:23], v[24:25]
	s_nop 0
	v_pk_add_f32 v[184:185], v[184:185], v[186:187]
	v_pk_add_f32 v[186:187], v[26:27], v[28:29]
	s_nop 0
	v_pk_add_f32 v[184:185], v[184:185], v[186:187]
	v_pk_add_f32 v[186:187], v[30:31], v[32:33]
	s_nop 0
	v_pk_add_f32 v[184:185], v[184:185], v[186:187]
	s_nop 0
	v_pk_mul_f32 v[184:185], v[184:185], s[92:93] op_sel_hi:[1,0]
	s_mov_b32 s92, 0x800000
	v_fma_f32 v155, -v184, v184, v185
	v_max_f32_e32 v155, 0, v155
	v_add_f32_e32 v155, 0x3727c5ac, v155
	v_mul_f32_e32 v157, 0x4b800000, v155
	v_cmp_gt_f32_e32 vcc, s92, v155
	s_nop 1
	v_cndmask_b32_e32 v155, v155, v157, vcc
	v_rsq_f32_e32 v155, v155
	s_nop 0
	v_mul_f32_e32 v157, 0x45800000, v155
	v_cndmask_b32_e32 v185, v155, v157, vcc
	ds_write_b64 v178, v[184:185]
.LBB0_814:
	s_or_b64 exec, exec, s[76:77]
	s_waitcnt vmcnt(7)
	ds_write_b64 v241, v[244:245]
	ds_write_b64 v241, v[246:247] offset:1024
	s_waitcnt lgkmcnt(0)
	s_barrier
	ds_read_b128 v[138:141], v240
	ds_read_b128 v[126:129], v240 offset:16
	ds_read_b128 v[118:121], v240 offset:32
	ds_read_b128 v[106:109], v240 offset:48
	ds_read_b128 v[98:101], v240 offset:64
	ds_read_b128 v[90:93], v240 offset:80
	ds_read_b128 v[78:81], v240 offset:96
	ds_read_b128 v[66:69], v240 offset:112
	ds_read_b128 v[142:145], v240 offset:1024
	ds_read_b128 v[134:137], v240 offset:1040
	ds_read_b128 v[122:125], v240 offset:1056
	ds_read_b128 v[114:117], v240 offset:1072
	ds_read_b128 v[102:105], v240 offset:1088
	ds_read_b128 v[94:97], v240 offset:1104
	ds_read_b128 v[82:85], v240 offset:1120
	ds_read_b128 v[70:73], v240 offset:1136
	ds_read_b64 v[184:185], v179
	s_waitcnt vmcnt(9)
	v_lshlrev_b32_e32 v155, 16, v130
	v_and_b32_e32 v130, 0xffff0000, v130
	s_waitcnt vmcnt(6)
	v_cndmask_b32_e64 v62, v62, 0, s[12:13]
	v_cndmask_b32_e64 v63, v63, 0, s[14:15]
	s_waitcnt lgkmcnt(0)
	v_sub_f32_e32 v155, v155, v184
	v_mul_f32_e32 v155, v185, v155
	v_fma_f32 v138, v138, v155, v142
	v_sub_f32_e32 v130, v130, v184
	v_bfe_u32 v142, v138, 16, 1
	v_mul_f32_e32 v130, v185, v130
	v_add3_u32 v138, v138, v142, s91
	v_fma_f32 v130, v139, v130, v143
	ds_write_b16_d16_hi v183, v138 offset:5376
	v_bfe_u32 v138, v130, 16, 1
	v_add3_u32 v130, v130, v138, s91
	ds_write_b16_d16_hi v183, v130 offset:5648
	v_lshlrev_b32_e32 v130, 16, v131
	v_sub_f32_e32 v130, v130, v184
	v_mul_f32_e32 v130, v185, v130
	v_fma_f32 v130, v140, v130, v144
	v_bfe_u32 v138, v130, 16, 1
	v_add3_u32 v130, v130, v138, s91
	ds_write_b16_d16_hi v183, v130 offset:5920
	v_and_b32_e32 v130, 0xffff0000, v131
	v_sub_f32_e32 v130, v130, v184
	v_mul_f32_e32 v130, v185, v130
	v_fmac_f32_e32 v145, v141, v130
	v_bfe_u32 v130, v145, 16, 1
	v_add3_u32 v130, v145, v130, s91
	ds_write_b16_d16_hi v183, v130 offset:6192
	v_lshlrev_b32_e32 v130, 16, v132
	v_sub_f32_e32 v130, v130, v184
	v_mul_f32_e32 v130, v185, v130
	v_fma_f32 v126, v126, v130, v134
	v_bfe_u32 v130, v126, 16, 1
	v_add3_u32 v126, v126, v130, s91
	ds_write_b16_d16_hi v183, v126 offset:1024
	v_and_b32_e32 v126, 0xffff0000, v132
	v_sub_f32_e32 v126, v126, v184
	v_mul_f32_e32 v126, v185, v126
	v_fma_f32 v126, v127, v126, v135
	v_bfe_u32 v127, v126, 16, 1
	v_add3_u32 v126, v126, v127, s91
	ds_write_b16_d16_hi v183, v126 offset:1296
	v_lshlrev_b32_e32 v126, 16, v133
	v_sub_f32_e32 v126, v126, v184
	v_mul_f32_e32 v126, v185, v126
	v_fma_f32 v126, v128, v126, v136
	v_bfe_u32 v127, v126, 16, 1
	v_add3_u32 v126, v126, v127, s91
	ds_write_b16_d16_hi v183, v126 offset:1568
	v_and_b32_e32 v126, 0xffff0000, v133
	v_sub_f32_e32 v126, v126, v184
	v_mul_f32_e32 v126, v185, v126
	v_fmac_f32_e32 v137, v129, v126
	v_bfe_u32 v126, v137, 16, 1
	v_add3_u32 v126, v137, v126, s91
	ds_write_b16_d16_hi v183, v126 offset:1840
	v_lshlrev_b32_e32 v126, 16, v110
	v_sub_f32_e32 v126, v126, v184
	v_mul_f32_e32 v126, v185, v126
	v_and_b32_e32 v110, 0xffff0000, v110
	v_fma_f32 v118, v118, v126, v122
; __device__ __forceinline__ unsigned f2bf(float f) { unsigned u = __builtin_bit_cast(unsigned, f); return (u + 0x7fffu + ((u >> 16) & 1u)) >> 16; }
; __device__ __forceinline__ unsigned cvt_pk_bf16(float lo, float hi) { unsigned r; asm volatile("v_cvt_pk_bf16_f32 %0, %1, %2" : "=v"(r) : "v"(lo), "v"(hi)); return r; }
; __device__ __forceinline__ void sg_phase(const Frame& F, const KArgs& a, const int u_first, const int u_count) {
;     ...
;         { const int s = s_; const f32x2 ms = st[s];
; #pragma unroll
;             for (int q = 0; q < 4; ++q) { const u32x4 raw = zraw[q]; const unsigned rw[4] = {raw.x, raw.y, raw.z, raw.w};
;                 const f32x4 g0 = lg[q][0], g1 = lg[q][1], b0 = lb[q][0], b1 = lb[q][1];
; #pragma unroll
;                 for (int i = 0; i < 8; ++i) { const unsigned wd = rw[i >> 1]; const float v = __builtin_bit_cast(float, (i & 1) ? (wd & 0xffff0000u) : (wd << 16));
;                     const float gg = (i < 4) ? g0[i & 3] : g1[i & 3], bb = (i < 4) ? b0[i & 3] : b1[i & 3];
;                     vt[(c0 + 8 * q + i) * 136 + (s ^ ((tid & 3) * 16))] = (unsigned short)f2bf((v - ms[0]) * ms[1] * gg + bb); } } }
;         __syncthreads();
;         f32x4 acc[8];
; #pragma unroll
;         for (int j = 0; j < 8; ++j) acc[j] = (f32x4){0.f, 0.f, 0.f, 0.f};
; #pragma unroll
;         for (int ks = 0; ks < 4; ++ks) { if (ks > (w >> 1)) continue;
;             const f32x4 w0 = wraw[ks][0], w1 = wraw[ks][1];
;             float wv[8] = {w0[0], w0[1], w0[2], w0[3], w1[0], w1[1], w1[2], w1[3]};
; #pragma unroll
;             for (int i = 0; i < 8; ++i) if (32 * ks + 8 * kq + i > t) wv[i] = 0.f;
;             u32x4 pk; pk.x = cvt_pk_bf16(wv[0], wv[1]); pk.y = cvt_pk_bf16(wv[2], wv[3]); pk.z = cvt_pk_bf16(wv[4], wv[5]); pk.w = cvt_pk_bf16(wv[6], wv[7]);
;             const bf16x8 wf = __builtin_bit_cast(bf16x8, pk);
	v_sub_f32_e32 v110, v110, v184
	v_bfe_u32 v122, v118, 16, 1
	v_mul_f32_e32 v110, v185, v110
	v_add3_u32 v118, v118, v122, s91
	v_fma_f32 v110, v119, v110, v123
	ds_write_b16_d16_hi v183, v118 offset:6464
	v_bfe_u32 v118, v110, 16, 1
	v_add3_u32 v110, v110, v118, s91
	ds_write_b16_d16_hi v183, v110 offset:6736
	v_lshlrev_b32_e32 v110, 16, v111
	v_sub_f32_e32 v110, v110, v184
	v_mul_f32_e32 v110, v185, v110
	v_fma_f32 v110, v120, v110, v124
	v_bfe_u32 v118, v110, 16, 1
	v_add3_u32 v110, v110, v118, s91
	ds_write_b16_d16_hi v183, v110 offset:7008
	v_and_b32_e32 v110, 0xffff0000, v111
	v_sub_f32_e32 v110, v110, v184
	v_mul_f32_e32 v110, v185, v110
	v_fmac_f32_e32 v125, v121, v110
	v_bfe_u32 v110, v125, 16, 1
	v_add3_u32 v110, v125, v110, s91
	ds_write_b16_d16_hi v183, v110 offset:7280
	v_lshlrev_b32_e32 v110, 16, v112
	v_sub_f32_e32 v110, v110, v184
	v_mul_f32_e32 v110, v185, v110
	v_fma_f32 v106, v106, v110, v114
	v_bfe_u32 v110, v106, 16, 1
	v_add3_u32 v106, v106, v110, s91
	ds_write_b16_d16_hi v183, v106 offset:2112
	v_and_b32_e32 v106, 0xffff0000, v112
	v_sub_f32_e32 v106, v106, v184
	v_mul_f32_e32 v106, v185, v106
	v_fma_f32 v106, v107, v106, v115
	v_bfe_u32 v107, v106, 16, 1
	v_add3_u32 v106, v106, v107, s91
	ds_write_b16_d16_hi v183, v106 offset:2384
	v_lshlrev_b32_e32 v106, 16, v113
	v_sub_f32_e32 v106, v106, v184
	v_mul_f32_e32 v106, v185, v106
	v_fma_f32 v106, v108, v106, v116
	v_bfe_u32 v107, v106, 16, 1
	v_add3_u32 v106, v106, v107, s91
	ds_write_b16_d16_hi v183, v106 offset:2656
	v_and_b32_e32 v106, 0xffff0000, v113
	v_sub_f32_e32 v106, v106, v184
	v_mul_f32_e32 v106, v185, v106
	v_fmac_f32_e32 v117, v109, v106
	v_bfe_u32 v106, v117, 16, 1
	v_add3_u32 v106, v117, v106, s91
	ds_write_b16_d16_hi v183, v106 offset:2928
	v_lshlrev_b32_e32 v106, 16, v86
	v_sub_f32_e32 v106, v106, v184
	v_mul_f32_e32 v106, v185, v106
	v_and_b32_e32 v86, 0xffff0000, v86
	v_fma_f32 v98, v98, v106, v102
	v_sub_f32_e32 v86, v86, v184
	v_bfe_u32 v102, v98, 16, 1
	v_mul_f32_e32 v86, v185, v86
	v_add3_u32 v98, v98, v102, s91
	v_fma_f32 v86, v99, v86, v103
	ds_write_b16_d16_hi v183, v98 offset:7552
	v_bfe_u32 v98, v86, 16, 1
	v_add3_u32 v86, v86, v98, s91
	ds_write_b16_d16_hi v183, v86 offset:7824
	v_lshlrev_b32_e32 v86, 16, v87
	v_sub_f32_e32 v86, v86, v184
	v_mul_f32_e32 v86, v185, v86
	v_fma_f32 v86, v100, v86, v104
	v_bfe_u32 v98, v86, 16, 1
	v_add3_u32 v86, v86, v98, s91
	ds_write_b16_d16_hi v183, v86 offset:8096
	v_and_b32_e32 v86, 0xffff0000, v87
	v_sub_f32_e32 v86, v86, v184
	v_mul_f32_e32 v86, v185, v86
	v_fmac_f32_e32 v105, v101, v86
	v_bfe_u32 v86, v105, 16, 1
	v_add3_u32 v86, v105, v86, s91
	ds_write_b16_d16_hi v183, v86 offset:8368
	v_lshlrev_b32_e32 v86, 16, v88
	v_sub_f32_e32 v86, v86, v184
	v_mul_f32_e32 v86, v185, v86
	v_fma_f32 v86, v90, v86, v94
	v_bfe_u32 v87, v86, 16, 1
	v_add3_u32 v86, v86, v87, s91
	ds_write_b16_d16_hi v183, v86 offset:3200
	v_and_b32_e32 v86, 0xffff0000, v88
	v_sub_f32_e32 v86, v86, v184
	v_mul_f32_e32 v86, v185, v86
	v_fma_f32 v86, v91, v86, v95
	v_bfe_u32 v87, v86, 16, 1
	v_add3_u32 v86, v86, v87, s91
	ds_write_b16_d16_hi v183, v86 offset:3472
	v_lshlrev_b32_e32 v86, 16, v89
	v_sub_f32_e32 v86, v86, v184
	v_mul_f32_e32 v86, v185, v86
	v_fma_f32 v86, v92, v86, v96
	v_bfe_u32 v87, v86, 16, 1
	v_add3_u32 v86, v86, v87, s91
	ds_write_b16_d16_hi v183, v86 offset:3744
	v_and_b32_e32 v86, 0xffff0000, v89
	v_sub_f32_e32 v86, v86, v184
	v_mul_f32_e32 v86, v185, v86
	v_fmac_f32_e32 v97, v93, v86
	v_bfe_u32 v86, v97, 16, 1
	v_add3_u32 v86, v97, v86, s91
	ds_write_b16_d16_hi v183, v86 offset:4016
	v_lshlrev_b32_e32 v86, 16, v58
	v_sub_f32_e32 v86, v86, v184
	v_mul_f32_e32 v86, v185, v86
	v_and_b32_e32 v58, 0xffff0000, v58
	v_fma_f32 v78, v78, v86, v82
	v_sub_f32_e32 v58, v58, v184
	v_bfe_u32 v82, v78, 16, 1
	v_mul_f32_e32 v58, v185, v58
	v_add3_u32 v78, v78, v82, s91
	v_fma_f32 v58, v79, v58, v83
	ds_write_b16_d16_hi v183, v78 offset:8640
	v_bfe_u32 v78, v58, 16, 1
	v_add3_u32 v58, v58, v78, s91
	ds_write_b16_d16_hi v183, v58 offset:8912
	v_lshlrev_b32_e32 v58, 16, v59
	v_sub_f32_e32 v58, v58, v184
	v_mul_f32_e32 v58, v185, v58
	v_fma_f32 v58, v80, v58, v84
	v_bfe_u32 v78, v58, 16, 1
	v_add3_u32 v58, v58, v78, s91
	ds_write_b16_d16_hi v183, v58 offset:9184
	v_and_b32_e32 v58, 0xffff0000, v59
	v_sub_f32_e32 v58, v58, v184
	v_mul_f32_e32 v58, v185, v58
	v_fmac_f32_e32 v85, v81, v58
	v_bfe_u32 v58, v85, 16, 1
	v_add3_u32 v58, v85, v58, s91
	ds_write_b16_d16_hi v183, v58 offset:9456
	v_lshlrev_b32_e32 v58, 16, v60
	v_sub_f32_e32 v58, v58, v184
	v_mul_f32_e32 v58, v185, v58
	v_fma_f32 v58, v66, v58, v70
	v_bfe_u32 v59, v58, 16, 1
	v_add3_u32 v58, v58, v59, s91
	ds_write_b16_d16_hi v183, v58 offset:4288
	v_and_b32_e32 v58, 0xffff0000, v60
	v_sub_f32_e32 v58, v58, v184
	v_mul_f32_e32 v58, v185, v58
	v_fma_f32 v58, v67, v58, v71
	v_bfe_u32 v59, v58, 16, 1
	v_add3_u32 v58, v58, v59, s91
	ds_write_b16_d16_hi v183, v58 offset:4560
	v_lshlrev_b32_e32 v58, 16, v61
	v_sub_f32_e32 v58, v58, v184
	v_mul_f32_e32 v58, v185, v58
	v_fma_f32 v58, v68, v58, v72
	v_bfe_u32 v59, v58, 16, 1
	v_add3_u32 v58, v58, v59, s91
	ds_write_b16_d16_hi v183, v58 offset:4832
	v_and_b32_e32 v58, 0xffff0000, v61
	v_sub_f32_e32 v58, v58, v184
	v_mul_f32_e32 v58, v185, v58
	v_fmac_f32_e32 v73, v69, v58
	v_bfe_u32 v58, v73, 16, 1
	v_add3_u32 v58, v73, v58, s91
	ds_write_b16_d16_hi v183, v58 offset:5104
	s_waitcnt vmcnt(5)
	v_cndmask_b32_e64 v58, v74, 0, s[4:5]
	v_cndmask_b32_e64 v59, 0, v75, s[6:7]
	v_cndmask_b32_e64 v58, v58, v74, s[6:7]
	v_cndmask_b32_e64 v60, v76, 0, s[8:9]
	v_cndmask_b32_e64 v61, v77, 0, s[10:11]
	v_cndmask_b32_e64 v64, v64, 0, s[16:17]
	v_cndmask_b32_e64 v65, v65, 0, s[18:19]
	s_waitcnt lgkmcnt(0)
	s_barrier
; #define LAS __attribute__((address_space(3)))
; __device__ __forceinline__ unsigned cvt_pk_bf16(float lo, float hi) { unsigned r; asm volatile("v_cvt_pk_bf16_f32 %0, %1, %2" : "=v"(r) : "v"(lo), "v"(hi)); return r; }
; __device__ __forceinline__ void sg_phase(const Frame& F, const KArgs& a, const int u_first, const int u_count) {
;     ...
; #pragma unroll
;         for (int ks = 0; ks < 4; ++ks) { if (ks > (w >> 1)) continue;
;             const f32x4 w0 = wraw[ks][0], w1 = wraw[ks][1];
;             float wv[8] = {w0[0], w0[1], w0[2], w0[3], w1[0], w1[1], w1[2], w1[3]};
; #pragma unroll
;             for (int i = 0; i < 8; ++i) if (32 * ks + 8 * kq + i > t) wv[i] = 0.f;
;             u32x4 pk; pk.x = cvt_pk_bf16(wv[0], wv[1]); pk.y = cvt_pk_bf16(wv[2], wv[3]); pk.z = cvt_pk_bf16(wv[4], wv[5]); pk.w = cvt_pk_bf16(wv[6], wv[7]);
;             const bf16x8 wf = __builtin_bit_cast(bf16x8, pk);
; #pragma unroll
;             for (int j = 0; j < 8; ++j) { const bf16x8 vf = *(const LAS bf16x8*)(vt + (16 * j + tl) * 136 + ((32 * ks + 8 * kq) ^ ((j >> 1) * 16)));
;                 acc[j] = __builtin_amdgcn_mfma_f32_16x16x32_bf16(vf, wf, acc[j], 0, 0, 0); }
;         }
	v_cvt_pk_bf16_f32 v58, v58, v59
	v_cvt_pk_bf16_f32 v59, v60, v61
	v_cvt_pk_bf16_f32 v60, v62, v63
	v_cvt_pk_bf16_f32 v61, v64, v65
	ds_read_b128 v[62:65], v180 offset:1024
	ds_read_b128 v[66:69], v180 offset:5376
	s_waitcnt lgkmcnt(1)
	v_mfma_f32_16x16x32_bf16 v[86:89], v[62:65], v[58:61], 0
	ds_read_b128 v[62:65], v181 offset:9728
	ds_read_b128 v[90:93], v181 offset:31552
	s_and_b64 vcc, exec, s[74:75]
	s_waitcnt lgkmcnt(2)
	v_mfma_f32_16x16x32_bf16 v[82:85], v[66:69], v[58:61], 0
	ds_read_b128 v[66:69], v181 offset:14080
	s_waitcnt lgkmcnt(2)
	v_mfma_f32_16x16x32_bf16 v[78:81], v[62:65], v[58:61], 0
	ds_read_b128 v[62:65], v180 offset:18496
	s_waitcnt lgkmcnt(1)
	v_mfma_f32_16x16x32_bf16 v[74:77], v[66:69], v[58:61], 0
	ds_read_b128 v[66:69], v180 offset:22848
	s_waitcnt lgkmcnt(1)
	v_mfma_f32_16x16x32_bf16 v[70:73], v[62:65], v[58:61], 0
	ds_read_b128 v[62:65], v181 offset:27200
	s_waitcnt lgkmcnt(1)
	v_mfma_f32_16x16x32_bf16 v[66:69], v[66:69], v[58:61], 0
	s_waitcnt lgkmcnt(0)
	v_mfma_f32_16x16x32_bf16 v[62:65], v[62:65], v[58:61], 0
	v_mfma_f32_16x16x32_bf16 v[58:61], v[90:93], v[58:61], 0
	s_cbranch_vccnz .LBB0_816
	v_readlane_b32 s36, v251, 7
	v_readlane_b32 s37, v251, 8
	v_cndmask_b32_e64 v53, v53, 0, s[94:95]
	v_cndmask_b32_e64 v92, v52, 0, s[34:35]
	v_cndmask_b32_e64 v54, v54, 0, s[36:37]
	v_readlane_b32 s36, v251, 16
	v_readlane_b32 s37, v251, 17
	s_nop 1
	v_cndmask_b32_e64 v55, v55, 0, s[36:37]
	v_readlane_b32 s36, v251, 22
	v_readlane_b32 s37, v251, 23
	s_nop 1
	v_cndmask_b32_e64 v56, v56, 0, s[36:37]
	v_readlane_b32 s36, v251, 24
	v_readlane_b32 s37, v251, 25
	s_nop 1
	v_cndmask_b32_e64 v57, v57, 0, s[36:37]
	v_readlane_b32 s36, v251, 26
	v_readlane_b32 s37, v251, 27
	s_nop 1
	v_cndmask_b32_e64 v90, v50, 0, s[36:37]
	v_readlane_b32 s36, v251, 28
	v_readlane_b32 s37, v251, 29
	v_cvt_pk_bf16_f32 v50, v54, v55
	s_nop 1
	v_cndmask_b32_e64 v91, v51, 0, s[36:37]
	v_cvt_pk_bf16_f32 v51, v56, v57
	v_cvt_pk_bf16_f32 v52, v90, v91
	v_cvt_pk_bf16_f32 v53, v92, v53
	ds_read_b128 v[2:5], v180 offset:1088
	ds_read_b128 v[6:9], v180 offset:5440
	ds_read_b128 v[10:13], v181 offset:9792
	ds_read_b128 v[14:17], v181 offset:14144
	ds_read_b128 v[18:21], v180 offset:18432
	ds_read_b128 v[22:25], v180 offset:22784
	ds_read_b128 v[26:29], v181 offset:27136
	ds_read_b128 v[30:33], v181 offset:31488
	s_waitcnt lgkmcnt(7)
	v_mfma_f32_16x16x32_bf16 v[86:89], v[2:5], v[50:53], v[86:89]
	s_waitcnt lgkmcnt(6)
	v_mfma_f32_16x16x32_bf16 v[82:85], v[6:9], v[50:53], v[82:85]
	s_waitcnt lgkmcnt(5)
	v_mfma_f32_16x16x32_bf16 v[78:81], v[10:13], v[50:53], v[78:81]
	s_waitcnt lgkmcnt(4)
	v_mfma_f32_16x16x32_bf16 v[74:77], v[14:17], v[50:53], v[74:77]
	s_waitcnt lgkmcnt(3)
	v_mfma_f32_16x16x32_bf16 v[70:73], v[18:21], v[50:53], v[70:73]
	s_waitcnt lgkmcnt(2)
	v_mfma_f32_16x16x32_bf16 v[66:69], v[22:25], v[50:53], v[66:69]
	s_waitcnt lgkmcnt(1)
	v_mfma_f32_16x16x32_bf16 v[62:65], v[26:29], v[50:53], v[62:65]
	s_waitcnt lgkmcnt(0)
	v_mfma_f32_16x16x32_bf16 v[58:61], v[30:33], v[50:53], v[58:61]
